# P1 idle tail converts 2048 more PEER table rows (taken from the HBM-bound P10)
# baseline (speedup 1.0000x reference)
; __device__ __forceinline__ void phase_peer_tables(const Frame& F, const Args& a, int r_lo, int r_hi, int gw, int NGW) {
;     unsigned char* PT = a.ws + WS_PT; const int lane = F.lane;
;     int r = r_lo + gw; if (r >= r_hi) return;
;     f32x4 vA[16], vB[16];
;     pt_load(a.in[17], a.in[18], vA, r, lane);
;     for (;;) {
;         const int r1 = r + NGW; const bool h1 = r1 < r_hi;
;         if (h1) pt_load(a.in[17], a.in[18], vB, r1, lane);
; __global__ void __launch_bounds__(NTHREADS, 2) fwd(Args args) {
;     ...
;         { const int nwg = (T / 256) * (ZW / 256), rem = nwg % F.G;
;           if (rem != 0 && F.vid >= rem) phase_peer_tables(F, args, side_rows, side_rows + PT_EARLY_ROWS, (F.vid - rem) * NWAVES + F.wave, (F.G - rem) * NWAVES);
;           else if (rem == 0) phase_peer_tables(F, args, side_rows, side_rows + PT_EARLY_ROWS, F.bid * NWAVES + F.wave, F.G * NWAVES); }
.LBB0_208:
	s_and_b64 s[0:1], s[0:1], exec
	s_cselect_b32 s10, 0x4000, 0
	s_abs_i32 s0, s96
	v_cvt_f32_u32_e32 v1, s0
	s_sub_i32 s1, 0, s0
	s_or_b32 s8, s10, 0x3800
	s_lshl_b32 s9, s96, 3
	v_rcp_iflag_f32_e32 v1, v1
	s_nop 0
	v_mul_f32_e32 v1, 0x4f7ffffe, v1
	v_cvt_u32_f32_e32 v1, v1
	s_nop 0
	v_readfirstlane_b32 s2, v1
	s_mul_i32 s1, s1, s2
	s_mul_hi_u32 s1, s2, s1
	s_add_i32 s2, s2, s1
	s_mul_hi_u32 s1, s2, 0x7a0
	s_mul_i32 s1, s1, s0
	s_sub_i32 s1, 0x7a0, s1
	s_sub_i32 s2, s1, s0
	s_cmp_ge_u32 s1, s0
	s_cselect_b32 s1, s2, s1
	s_sub_i32 s2, s1, s0
	s_cmp_ge_u32 s1, s0
	s_cselect_b32 s0, s2, s1
	s_cmp_eq_u32 s0, 0
	s_cbranch_scc1 .LBB0_224
	s_cmp_lt_i32 s84, s0
	s_cbranch_scc1 .LBB0_223
	s_sub_i32 s1, s84, s0
	s_lshl_b32 s1, s1, 3
	v_readlane_b32 s2, v245, 7
	s_add_i32 s1, s1, s2
	s_cmpk_gt_u32 s1, 0x37ff
	s_cbranch_scc1 .LBB0_223
	s_or_b32 s2, s1, s10
	s_cmpk_lt_u32 s2, 0x4000
	s_cselect_b32 s4, s13, s15
	s_cselect_b32 s5, s12, s14
	s_lshl_b32 s2, s1, 12
	s_mov_b32 s3, 0
	s_lshl_b64 s[2:3], s[2:3], 2
	s_add_u32 s2, s5, s2
	v_mov_b32_e32 v133, 0
	s_addc_u32 s3, s4, s3
	v_lshlrev_b32_e32 v130, 4, v194
	v_mov_b32_e32 v131, v133
	v_lshl_add_u64 v[26:27], s[2:3], 0, v[130:131]
	s_movk_i32 s11, 0x1000
	v_add_co_u32_e32 v66, vcc, s11, v26
	s_movk_i32 s1, 0x2000
	s_nop 0
	v_addc_co_u32_e32 v67, vcc, 0, v27, vcc
	v_add_co_u32_e32 v28, vcc, s1, v26
	global_load_dwordx4 v[2:5], v130, s[2:3] offset:1024
	global_load_dwordx4 v[6:9], v130, s[2:3] offset:2048
	v_addc_co_u32_e32 v29, vcc, 0, v27, vcc
	global_load_dwordx4 v[10:13], v130, s[2:3] offset:3072
	global_load_dwordx4 v[14:17], v[28:29], off offset:-4096
	global_load_dwordx4 v[18:21], v[66:67], off offset:1024
	global_load_dwordx4 v[22:25], v[66:67], off offset:2048
	global_load_dwordx4 v[30:33], v[28:29], off
	global_load_dwordx4 v[34:37], v[28:29], off offset:1024
	global_load_dwordx4 v[42:45], v[28:29], off offset:2048
	global_load_dwordx4 v[46:49], v[28:29], off offset:3072
	s_movk_i32 s1, 0x3000
	v_add_co_u32_e32 v68, vcc, s1, v26
	v_mbcnt_lo_u32_b32 v1, -1, 0
	s_nop 0
	v_addc_co_u32_e32 v69, vcc, 0, v27, vcc
	global_load_dwordx4 v[38:41], v[66:67], off offset:3072
	global_load_dwordx4 v[50:53], v[68:69], off
	global_load_dwordx4 v[54:57], v[68:69], off offset:1024
	global_load_dwordx4 v[58:61], v[68:69], off offset:2048
	global_load_dwordx4 v[26:29], v130, s[2:3]
	global_load_dwordx4 v[62:65], v[68:69], off offset:3072
	v_mbcnt_hi_u32_b32 v66, -1, v1
	v_and_b32_e32 v1, 64, v66
	v_add_u32_e32 v67, 64, v1
	v_xor_b32_e32 v1, 1, v66
	v_cmp_lt_i32_e32 vcc, v1, v67
	v_xor_b32_e32 v68, 2, v66
	v_readlane_b32 s21, v245, 7
	v_cndmask_b32_e32 v1, v66, v1, vcc
	v_cmp_lt_i32_e32 vcc, v68, v67
	s_add_i32 s1, s10, s21
	s_lshl_b32 s2, s0, 3
	v_cndmask_b32_e32 v68, v66, v68, vcc
	v_lshlrev_b32_e32 v136, 2, v68
	v_xor_b32_e32 v68, 4, v66
	v_cmp_lt_i32_e32 vcc, v68, v67
	s_sub_i32 s17, s1, s2
	s_lshl_b32 s2, s96, 4
	v_cndmask_b32_e32 v68, v66, v68, vcc
	v_lshlrev_b32_e32 v137, 2, v68
	v_xor_b32_e32 v68, 8, v66
	v_cmp_lt_i32_e32 vcc, v68, v67
	s_lshl_b32 s3, s0, 4
	s_sub_i32 s18, s2, s3
	v_cndmask_b32_e32 v68, v66, v68, vcc
	v_lshlrev_b32_e32 v138, 2, v68
	v_xor_b32_e32 v68, 16, v66
	v_cmp_lt_i32_e32 vcc, v68, v67
	s_add_i32 s2, s1, s2
	s_mul_i32 s4, s0, 24
	v_cndmask_b32_e32 v68, v66, v68, vcc
	v_lshlrev_b32_e32 v139, 2, v68
	v_xor_b32_e32 v68, 32, v66
	s_sub_i32 s19, s2, s4
	s_lshl_b32 s2, s96, 16
	s_mul_i32 s4, s0, 0x18000
	v_cmp_lt_i32_e32 vcc, v68, v67
	s_sub_i32 s20, s2, s4
	s_lshl_b32 s4, s84, 15
	s_lshl_b32 s5, s10, 12
	s_add_i32 s1, s1, s9
	v_cndmask_b32_e32 v66, v66, v68, vcc
	s_add_i32 s4, s4, s5
	s_lshl_b32 s5, s21, 12
	s_lshl_b32 s0, s0, 16
	s_sub_i32 s23, s1, s3
	s_lshl_b32 s1, s96, 15
	v_lshlrev_b32_e32 v1, 2, v1
	v_lshlrev_b32_e32 v140, 2, v66
	s_lshl_b32 s16, s84, 3
	s_add_i32 s21, s4, s5
	s_sub_i32 s22, s2, s0
	s_sub_i32 s24, s1, s0
	s_mov_b32 s25, 0x42fe0000
	s_mov_b32 s26, 0x40c0c00
	s_mov_b32 s27, 0x400000
	s_mov_b32 s28, 0x800000
	s_mov_b32 s29, 0xc00000
	s_mov_b32 s30, 0x1000000
	s_mov_b32 s31, 0x1400000
	s_mov_b32 s34, 0x1800000
	s_mov_b32 s35, 0x1c00000
	s_brev_b32 s36, 64
	s_mov_b32 s37, 0x2400000
	s_mov_b32 s38, 0x2800000
	s_mov_b32 s39, 0x2c00000
	s_mov_b32 s40, 0x3000000
	s_mov_b32 s41, 0x3400000
	s_mov_b32 s42, 0x3800000
	s_brev_b32 s43, 16
	s_branch .LBB0_214

; __device__ __forceinline__ void phase_peer_tables(const Frame& F, const Args& a, int r_lo, int r_hi, int gw, int NGW) {
;     unsigned char* PT = a.ws + WS_PT; const int lane = F.lane;
;     int r = r_lo + gw; if (r >= r_hi) return;
;     f32x4 vA[16], vB[16];
;     pt_load(a.in[17], a.in[18], vA, r, lane);
;     for (;;) {
;         const int r1 = r + NGW; const bool h1 = r1 < r_hi;
;         if (h1) pt_load(a.in[17], a.in[18], vB, r1, lane);
; __global__ void __launch_bounds__(NTHREADS, 2) fwd(Args args) {
;     ...
;           else if (rem == 0) phase_peer_tables(F, args, side_rows, side_rows + PT_EARLY_ROWS, F.bid * NWAVES + F.wave, F.G * NWAVES); }
.LBB0_224:
.LBB0_225:
	s_lshl_b32 s0, s94, 3
	v_readlane_b32 s1, v245, 7
	s_add_i32 s0, s1, s0
	s_cmpk_gt_i32 s0, 0x37ff
	s_cbranch_scc1 .LBB0_238
	s_add_i32 s39, s10, s0
	s_cmpk_lt_u32 s39, 0x4000
	s_cselect_b32 s1, s13, s15
	s_cselect_b32 s2, s12, s14
	s_lshl_b32 s0, s0, 14
	s_and_b32 s0, s0, 0xfffc000
	s_add_u32 s0, s2, s0
	v_mov_b32_e32 v133, 0
	s_addc_u32 s1, s1, 0
	v_lshlrev_b32_e32 v130, 4, v194
	v_mov_b32_e32 v131, v133
	s_waitcnt vmcnt(31)
	v_lshl_add_u64 v[26:27], s[0:1], 0, v[130:131]
	s_movk_i32 s11, 0x1000
	v_add_co_u32_e32 v66, vcc, s11, v26
	s_movk_i32 s2, 0x2000
	s_nop 0
	v_addc_co_u32_e32 v67, vcc, 0, v27, vcc
	v_add_co_u32_e32 v28, vcc, s2, v26
	global_load_dwordx4 v[2:5], v130, s[0:1] offset:1024
	global_load_dwordx4 v[6:9], v130, s[0:1] offset:2048
	v_addc_co_u32_e32 v29, vcc, 0, v27, vcc
	global_load_dwordx4 v[10:13], v130, s[0:1] offset:3072
	global_load_dwordx4 v[14:17], v[28:29], off offset:-4096
	global_load_dwordx4 v[18:21], v[66:67], off offset:1024
	global_load_dwordx4 v[22:25], v[66:67], off offset:2048
	global_load_dwordx4 v[30:33], v[28:29], off
	global_load_dwordx4 v[34:37], v[28:29], off offset:1024
	global_load_dwordx4 v[42:45], v[28:29], off offset:2048
	global_load_dwordx4 v[46:49], v[28:29], off offset:3072
	s_movk_i32 s2, 0x3000
	v_add_co_u32_e32 v68, vcc, s2, v26
	v_mbcnt_lo_u32_b32 v1, -1, 0
	s_nop 0
	v_addc_co_u32_e32 v69, vcc, 0, v27, vcc
	global_load_dwordx4 v[38:41], v[66:67], off offset:3072
	global_load_dwordx4 v[50:53], v[68:69], off
	global_load_dwordx4 v[54:57], v[68:69], off offset:1024
	global_load_dwordx4 v[58:61], v[68:69], off offset:2048
	global_load_dwordx4 v[26:29], v130, s[0:1]
	global_load_dwordx4 v[62:65], v[68:69], off offset:3072
	v_mbcnt_hi_u32_b32 v66, -1, v1
	v_and_b32_e32 v1, 64, v66
	v_add_u32_e32 v67, 64, v1
	v_xor_b32_e32 v1, 1, v66
	v_cmp_lt_i32_e32 vcc, v1, v67
	v_xor_b32_e32 v68, 2, v66
	s_lshl_b32 s0, s94, 15
	v_cndmask_b32_e32 v1, v66, v1, vcc
	v_cmp_lt_i32_e32 vcc, v68, v67
	s_lshl_b32 s1, s10, 12
	s_add_i32 s0, s0, s1
	v_cndmask_b32_e32 v68, v66, v68, vcc
	v_lshlrev_b32_e32 v136, 2, v68
	v_xor_b32_e32 v68, 4, v66
	v_cmp_lt_i32_e32 vcc, v68, v67
	v_readlane_b32 s1, v245, 7
	s_lshl_b32 s1, s1, 12
	v_cndmask_b32_e32 v68, v66, v68, vcc
	v_lshlrev_b32_e32 v137, 2, v68
	v_xor_b32_e32 v68, 8, v66
	v_cmp_lt_i32_e32 vcc, v68, v67
	v_lshlrev_b32_e32 v1, 2, v1
	s_lshl_b32 s16, s96, 4
	v_cndmask_b32_e32 v68, v66, v68, vcc
	v_lshlrev_b32_e32 v138, 2, v68
	v_xor_b32_e32 v68, 16, v66
	v_cmp_lt_i32_e32 vcc, v68, v67
	s_lshl_b32 s17, s96, 16
	s_add_i32 s10, s0, s1
	v_cndmask_b32_e32 v68, v66, v68, vcc
	v_lshlrev_b32_e32 v139, 2, v68
	v_xor_b32_e32 v68, 32, v66
	v_cmp_lt_i32_e32 vcc, v68, v67
	s_lshl_b32 s18, s96, 15
	s_mov_b32 s19, 0x42fe0000
	v_cndmask_b32_e32 v66, v66, v68, vcc
	v_lshlrev_b32_e32 v140, 2, v66
	s_mov_b32 s20, 0x40c0c00
	s_mov_b32 s21, 0x400000
	s_mov_b32 s22, 0x800000
	s_mov_b32 s23, 0xc00000
	s_mov_b32 s24, 0x1000000
	s_mov_b32 s25, 0x1400000
	s_mov_b32 s26, 0x1800000
	s_mov_b32 s27, 0x1c00000
	s_brev_b32 s28, 64
	s_mov_b32 s29, 0x2400000
	s_mov_b32 s30, 0x2800000
	s_mov_b32 s31, 0x2c00000
	s_mov_b32 s34, 0x3000000
	s_mov_b32 s35, 0x3400000
	s_mov_b32 s36, 0x3800000
	s_brev_b32 s37, 16
	s_branch .LBB0_229

; __device__ __forceinline__ void phase_peer_tables(const Frame& F, const Args& a, int r_lo, int r_hi, int gw, int NGW) {
;     unsigned char* PT = a.ws + WS_PT; const int lane = F.lane;
;     int r = r_lo + gw; if (r >= r_hi) return;
;     f32x4 vA[16], vB[16];
;     pt_load(a.in[17], a.in[18], vA, r, lane);
;     for (;;) {
;         const int r1 = r + NGW; const bool h1 = r1 < r_hi;
;         if (h1) pt_load(a.in[17], a.in[18], vB, r1, lane);
; __global__ void __launch_bounds__(NTHREADS, 2) fwd(Args args) {
;     ...
;         phase_peer_tables(F, args, ((F.G == 256) ? PT_SIDE_ROWS : 0) + PT_EARLY_ROWS, 32768, F.bid * NWAVES + F.wave, F.G * NWAVES);
.LBB0_1248:
	s_cmpk_eq_i32 s96, 0x100
	s_movk_i32 s1, 0x7800
	s_cselect_b32 s5, s1, 0x3800
	s_add_i32 s41, s5, s4
	s_cmpk_gt_i32 s41, 0x7fff
	s_movk_i32 s4, 0x3000
	s_cbranch_scc1 .LBB0_1261
	s_add_u32 s1, s2, 0x3ba00000
	s_addc_u32 s10, s3, 0
	s_cmpk_lt_u32 s41, 0x4000
	s_cselect_b32 s3, s13, s15
	s_cselect_b32 s2, s12, s14
	s_lshl_b32 s8, s41, 14
	s_and_b32 s8, s8, 0xfffc000
	s_add_u32 s2, s2, s8
	v_mov_b32_e32 v133, 0
	s_addc_u32 s3, s3, 0
	v_lshlrev_b32_e32 v130, 4, v194
	v_mov_b32_e32 v131, v133
	v_lshl_add_u64 v[26:27], s[2:3], 0, v[130:131]
	s_movk_i32 s11, 0x1000
	v_add_co_u32_e32 v66, vcc, s11, v26
	s_movk_i32 s8, 0x2000
	s_nop 0
	v_addc_co_u32_e32 v67, vcc, 0, v27, vcc
	v_add_co_u32_e32 v28, vcc, s8, v26
	global_load_dwordx4 v[2:5], v130, s[2:3] offset:1024
	global_load_dwordx4 v[6:9], v130, s[2:3] offset:2048
	v_addc_co_u32_e32 v29, vcc, 0, v27, vcc
	global_load_dwordx4 v[10:13], v130, s[2:3] offset:3072
	global_load_dwordx4 v[14:17], v[28:29], off offset:-4096
	global_load_dwordx4 v[18:21], v[66:67], off offset:1024
	global_load_dwordx4 v[22:25], v[66:67], off offset:2048
	global_load_dwordx4 v[30:33], v[28:29], off
	global_load_dwordx4 v[38:41], v[28:29], off offset:1024
	global_load_dwordx4 v[42:45], v[28:29], off offset:2048
	global_load_dwordx4 v[46:49], v[28:29], off offset:3072
	v_add_co_u32_e32 v68, vcc, s4, v26
	v_mbcnt_lo_u32_b32 v1, -1, 0
	s_nop 0
	v_addc_co_u32_e32 v69, vcc, 0, v27, vcc
	global_load_dwordx4 v[34:37], v[66:67], off offset:3072
	global_load_dwordx4 v[50:53], v[68:69], off
	global_load_dwordx4 v[54:57], v[68:69], off offset:1024
	global_load_dwordx4 v[58:61], v[68:69], off offset:2048
	global_load_dwordx4 v[26:29], v130, s[2:3]
	global_load_dwordx4 v[62:65], v[68:69], off offset:3072
	v_mbcnt_hi_u32_b32 v66, -1, v1
	v_and_b32_e32 v1, 64, v66
	v_add_u32_e32 v67, 64, v1
	v_xor_b32_e32 v1, 1, v66
	v_cmp_lt_i32_e32 vcc, v1, v67
	v_xor_b32_e32 v68, 2, v66
	s_lshl_b32 s2, s94, 15
	v_cndmask_b32_e32 v1, v66, v1, vcc
	v_cmp_lt_i32_e32 vcc, v68, v67
	s_lshl_b32 s3, s5, 12
	s_add_i32 s2, s2, s3
	v_cndmask_b32_e32 v68, v66, v68, vcc
	v_lshlrev_b32_e32 v136, 2, v68
	v_xor_b32_e32 v68, 4, v66
	v_cmp_lt_i32_e32 vcc, v68, v67
	v_readlane_b32 s3, v245, 7
	s_lshl_b32 s3, s3, 12
	v_cndmask_b32_e32 v68, v66, v68, vcc
	v_lshlrev_b32_e32 v137, 2, v68
	v_xor_b32_e32 v68, 8, v66
	v_cmp_lt_i32_e32 vcc, v68, v67
	v_lshlrev_b32_e32 v1, 2, v1
	s_lshl_b32 s16, s96, 4
	v_cndmask_b32_e32 v68, v66, v68, vcc
	v_lshlrev_b32_e32 v138, 2, v68
	v_xor_b32_e32 v68, 16, v66
	v_cmp_lt_i32_e32 vcc, v68, v67
	s_lshl_b32 s17, s96, 16
	s_add_i32 s20, s2, s3
	v_cndmask_b32_e32 v68, v66, v68, vcc
	v_lshlrev_b32_e32 v139, 2, v68
	v_xor_b32_e32 v68, 32, v66
	v_cmp_lt_i32_e32 vcc, v68, v67
	s_lshl_b32 s21, s96, 15
	s_mov_b32 s22, 0x42fe0000
	v_cndmask_b32_e32 v66, v66, v68, vcc
	v_lshlrev_b32_e32 v140, 2, v66
	s_mov_b32 s23, 0x40c0c00
	s_mov_b32 s24, 0x400000
	s_mov_b32 s25, 0x800000
	s_mov_b32 s26, 0xc00000
	s_mov_b32 s27, 0x1000000
	s_mov_b32 s28, 0x1400000
	s_mov_b32 s29, 0x1800000
	s_mov_b32 s30, 0x1c00000
	s_brev_b32 s31, 64
	s_mov_b32 s33, 0x2400000
	s_mov_b32 s34, 0x2800000
	s_mov_b32 s35, 0x2c00000
	s_mov_b32 s36, 0x3000000
	s_mov_b32 s37, 0x3400000
	s_mov_b32 s38, 0x3800000
	s_brev_b32 s39, 16
	s_branch .LBB0_1252
